# GQA attention: one static s_setprio 1 for waves 0-3 over the GQA sub-phase (reset after), on top of v44
# speedup vs baseline: 1.0013x; 1.0013x over previous
.LBB0_837:
	v_readlane_b32 s2, v255, 35
	v_readlane_b32 s3, v255, 36
	s_and_b64 s[2:3], s[2:3], exec
	s_movk_i32 s2, 0x120
	s_cselect_b32 s10, 0x100, s2
	s_cmp_ge_i32 s92, s10
	s_cbranch_scc1 .LBB0_862
	s_cmpk_ge_u32 s66, 0x100
	s_cbranch_scc1 .Lmy_gqa_prio
	s_setprio 1
.Lmy_gqa_prio:
	s_add_u32 s11, s44, 0x6a858000
	s_addc_u32 s12, s45, 0
	s_add_u32 s13, s44, 0x6bfd8000
	s_addc_u32 s14, s45, 0
	s_add_u32 s15, s44, 0x24118000
	s_addc_u32 s16, s45, 0
	v_and_b32_e32 v4, 0x3fffffc0, v0
	s_add_i32 s2, 0, 0x10000
	v_lshl_add_u32 v168, v4, 2, s2
	v_ashrrev_i32_e32 v5, 1, v0
	s_movk_i32 s2, 0xffe0
	v_ashrrev_i32_e32 v148, 4, v0
	v_and_b32_e32 v4, 0xffffffe0, v5
	v_bfi_b32 v5, s2, v5, v0
	s_movk_i32 s2, 0xa00
	v_and_b32_e32 v8, 0xfffff0, v148
	v_lshlrev_b32_e32 v9, 1, v148
	v_mad_i64_i32 v[146:147], s[2:3], v5, s2, 0
	v_lshlrev_b32_e32 v5, 3, v0
	v_and_or_b32 v8, v9, 8, v8
	v_and_b32_e32 v7, 0x78, v5
	v_lshrrev_b32_e32 v9, 1, v148
	v_lshrrev_b32_e32 v8, 1, v8
	v_bfe_u32 v5, v5, 5, 2
	v_and_b32_e32 v10, 3, v148
	v_or_b32_e32 v8, v8, v5
	v_and_or_b32 v9, v9, 4, v10
	v_lshlrev_b32_e32 v10, 1, v7
	v_lshlrev_b32_e32 v8, 9, v8
	v_lshlrev_b32_e32 v9, 6, v9
	v_and_b32_e32 v11, 48, v10
	v_or3_b32 v12, v8, v9, v11
	v_add_u32_e32 v8, 32, v148
	v_and_b32_e32 v13, 0xfffff0, v8
	v_lshlrev_b32_e32 v14, 1, v8
	v_and_or_b32 v13, v14, 8, v13
	v_lshrrev_b32_e32 v13, 1, v13
	v_or_b32_e32 v5, v13, v5
	v_and_b32_e32 v1, 63, v0
	v_lshlrev_b32_e32 v5, 9, v5
	v_lshlrev_b32_e32 v13, 4, v0
	v_or3_b32 v11, v5, v9, v11
	v_lshlrev_b32_e32 v5, 3, v1
	v_and_b32_e32 v9, 0xc0, v13
	v_lshlrev_b32_e32 v14, 1, v0
	v_and_or_b32 v9, v5, 24, v9
	v_and_b32_e32 v14, 32, v14
	v_and_b32_e32 v5, 0x100, v5
	v_or3_b32 v5, v9, v14, v5
	v_ashrrev_i32_e32 v149, 31, v148
	v_ashrrev_i32_e32 v9, 31, v8
	v_bfe_u32 v3, v0, 5, 1
	s_cmp_lg_u32 0, -1
	v_lshlrev_b64 v[150:151], 9, v[148:149]
	v_lshlrev_b64 v[152:153], 9, v[8:9]
	v_and_b32_e32 v2, 31, v0
	s_cselect_b32 s4, 0, 0
	v_or_b32_e32 v150, v150, v7
	v_or_b32_e32 v152, v152, v7
	v_lshlrev_b32_e32 v7, 8, v148
	v_and_b32_e32 v9, 0x70, v0
	v_lshlrev_b32_e32 v8, 8, v8
	v_lshlrev_b32_e32 v170, 4, v3
	s_mov_b64 s[2:3], 0x8000
	v_and_b32_e32 v0, 15, v0
	v_add_u32_e32 v169, s4, v5
	v_bitop3_b32 v7, v10, v7, v9 bitop3:0xde
	v_bitop3_b32 v8, v10, v8, v9 bitop3:0xde
	v_lshlrev_b32_e32 v9, 8, v2
	v_and_b32_e32 v10, 0x70, v13
	v_or_b32_e32 v14, 32, v170
	v_or_b32_e32 v15, 64, v170
	v_or_b32_e32 v16, 0x60, v170
	v_or_b32_e32 v17, 0x80, v170
	v_or_b32_e32 v18, 0xa0, v170
	v_or_b32_e32 v19, 0xc0, v170
	v_or_b32_e32 v20, 0xe0, v170
	v_lshl_add_u64 v[154:155], v[150:151], 0, s[2:3]
	s_mov_b64 s[2:3], 0xc000
	s_addk_i32 s4, 0x4000
	v_lshlrev_b32_e32 v96, 4, v0
	v_lshlrev_b32_e32 v6, 3, v3
	v_bitop3_b32 v13, v170, v9, v10 bitop3:0xde
	v_bitop3_b32 v14, v14, v9, v10 bitop3:0xde
	v_bitop3_b32 v15, v15, v9, v10 bitop3:0xde
	v_bitop3_b32 v16, v16, v9, v10 bitop3:0xde
	v_bitop3_b32 v17, v17, v9, v10 bitop3:0xde
	v_bitop3_b32 v18, v18, v9, v10 bitop3:0xde
	v_bitop3_b32 v19, v19, v9, v10 bitop3:0xde
	v_bitop3_b32 v9, v20, v9, v10 bitop3:0xde
	v_lshl_add_u64 v[156:157], v[150:151], 0, s[2:3]
	v_cmp_gt_u32_e64 s[2:3], 32, v1
	v_add_u32_e32 v172, s4, v5
	v_ashrrev_i32_e32 v5, 31, v4
	v_lshl_add_u64 v[0:1], s[44:45], 0, v[96:97]
	s_mov_b64 s[4:5], 0x6bff8000
	v_lshl_add_u32 v171, v2, 2, v168
	v_lshlrev_b64 v[158:159], 11, v[4:5]
	v_lshlrev_b32_e32 v160, 13, v3
	v_mov_b32_e32 v161, v97
	v_lshl_add_u64 v[162:163], v[0:1], 0, s[4:5]
	v_lshlrev_b32_e32 v164, 1, v6
	v_lshlrev_b32_e32 v96, 1, v2
	v_add_u32_e32 v173, 0, v12
	v_add_u32_e32 v174, 0, v11
	v_add_u32_e32 v175, 0, v7
	v_add_u32_e32 v176, 0, v8
	v_add_u32_e32 v177, 0, v13
	v_add_u32_e32 v178, 0, v14
	v_add_u32_e32 v179, 0, v15
	v_add_u32_e32 v180, 0, v16
	v_add_u32_e32 v181, 0, v17
	v_add_u32_e32 v182, 0, v18
	v_add_u32_e32 v183, 0, v19
	v_add_u32_e32 v184, 0, v9
	s_branch .LBB0_840

.LBB0_862:
	s_setprio 0
	v_mbcnt_lo_u32_b32 v0, -1, 0
	v_mbcnt_hi_u32_b32 v0, -1, v0
	v_readlane_b32 s4, v255, 44
	v_or_b32_e32 v1, s66, v0
	v_readlane_b32 s5, v255, 45
	v_readfirstlane_b32 s2, v1
	s_mov_b32 s3, s71
	s_ashr_i32 s2, s2, 6
	s_andn2_b64 vcc, exec, s[4:5]
	s_movk_i32 s28, 0x800
	s_cbranch_vccnz .LBB0_864
	v_readlane_b32 s8, v254, 53
	s_cmp_ge_i32 s3, s8
	s_cselect_b64 s[4:5], -1, 0
	s_cmp_lt_i32 s2, 2
	s_cselect_b64 s[6:7], -1, 0
	s_and_b64 s[4:5], s[4:5], s[6:7]
	s_sub_i32 s6, s3, s8
	s_lshl_b32 s6, s6, 1
	s_add_i32 s6, s2, s6
	s_addk_i32 s6, 0x800
	s_and_b64 s[4:5], s[4:5], exec
	s_cselect_b32 s28, s6, 0x900
